# router: loop-invariant router-bias loads hoisted out of the token-group loop (their in-order vmcnt waits drained the previous group's stores)
# baseline (speedup 1.0000x reference)
.LBB0_1026:
	s_or_b64 exec, exec, s[0:1]
	v_readlane_b32 s0, v254, 12
	v_readlane_b32 s1, v254, 13
	s_andn2_b64 vcc, exec, s[0:1]
	s_cbranch_vccnz .LBB0_1223
	v_readlane_b32 s0, v253, 3
	v_readlane_b32 s1, v253, 4
	s_load_dword s26, s[0:1], 0x0
	v_readlane_b32 s0, v254, 60
	s_mov_b32 s18, s0
	s_lshl_b32 s56, s18, 13
	s_lshl_b32 s0, s0, 8
	s_lshl_b64 s[14:15], s[56:57], 2
	s_add_u32 s9, s12, s14
	v_readlane_b32 s1, v254, 61
	s_addc_u32 s11, s13, s15
	s_mov_b32 s1, s57
	s_add_u32 s16, s9, 0x10000
	s_addc_u32 s17, s11, 0
	s_ashr_i32 s14, s2, 6
	s_lshl_b64 s[0:1], s[0:1], 2
	s_add_u32 s0, s3, s0
	s_addc_u32 s1, s8, s1
	s_lshl_b32 s2, s18, 19
	s_add_u32 s3, s12, s2
	s_addc_u32 s11, s13, 0
	v_and_b32_e32 v152, 63, v0
	s_add_u32 s8, s12, 0xa020000
	v_ashrrev_i32_e32 v6, 3, v0
	v_and_b32_e32 v12, 7, v0
	v_readlane_b32 s15, v254, 52
	s_addc_u32 s9, s13, 0
	s_lshl_b32 s18, s14, 3
	v_lshlrev_b32_e32 v2, 4, v152
	v_mov_b32_e32 v3, v1
	v_lshl_add_u32 v153, v6, 2, s15
	v_lshlrev_b32_e32 v8, 4, v12
	v_mov_b32_e32 v9, v1
	s_ashr_i32 s15, s14, 31
	s_ashr_i32 s19, s18, 31
	v_lshl_add_u64 v[4:5], s[8:9], 0, v[2:3]
	s_lshl_b32 s2, s14, 5
	s_waitcnt vmcnt(0)
	v_lshl_add_u64 v[104:105], s[8:9], 0, v[8:9]
	s_lshl_b64 s[8:9], s[14:15], 16
	s_add_u32 s8, s3, s8
	s_addc_u32 s9, s11, s9
	v_lshl_add_u64 v[2:3], s[8:9], 0, v[2:3]
	s_mov_b64 s[8:9], 0x517e0a00
	v_lshl_add_u64 v[106:107], v[2:3], 0, s[8:9]
	s_mov_b64 s[8:9], 0x518e0a00
	v_lshl_add_u64 v[108:109], v[2:3], 0, s[8:9]
	s_mov_b64 s[8:9], 0x517e1a00
	s_add_u32 s30, s12, 0x20000
	v_lshl_add_u64 v[110:111], v[2:3], 0, s[8:9]
	s_mov_b64 s[8:9], 0x518e1a00
	s_addc_u32 s31, s13, 0
	v_lshl_add_u64 v[112:113], v[2:3], 0, s[8:9]
	s_mov_b64 s[8:9], 0x517e1e00
	s_add_u32 s34, s12, 0x4ffe0a00
	s_movk_i32 s3, 0x90
	v_lshl_add_u64 v[114:115], v[2:3], 0, s[8:9]
	s_mov_b64 s[8:9], 0x518e1e00
	v_and_b32_e32 v10, 31, v0
	v_bfe_u32 v11, v0, 5, 1
	v_lshlrev_b32_e32 v0, 3, v12
	v_lshlrev_b32_e32 v154, 5, v12
	s_addc_u32 s35, s13, 0
	v_mul_lo_u32 v12, v6, s3
	s_lshl_b32 s3, s14, 7
	v_lshl_add_u64 v[116:117], v[2:3], 0, s[8:9]
	s_mov_b64 s[8:9], 0x517e2200
	s_add_i32 s3, s3, 0
	v_lshl_add_u64 v[118:119], v[2:3], 0, s[8:9]
	s_mov_b64 s[8:9], 0x518e2200
	s_add_u32 s36, s12, 0x2e360000
	v_lshl_add_u64 v[120:121], v[2:3], 0, s[8:9]
	s_mov_b64 s[8:9], 0x517e2600
	s_addc_u32 s37, s13, 0
	v_lshl_add_u64 v[122:123], v[2:3], 0, s[8:9]
	s_mov_b64 s[8:9], 0x518e2600
	s_add_u32 s48, s12, 0x2e3e0000
	v_lshl_add_u64 v[124:125], v[2:3], 0, s[8:9]
	v_lshlrev_b32_e32 v2, 2, v152
	v_mov_b32_e32 v3, v1
	s_addc_u32 s49, s13, 0
	v_lshl_add_u64 v[126:127], s[0:1], 0, v[2:3]
	global_load_dword v190, v[126:127], off
	global_load_dword v191, v[126:127], off offset:256
	global_load_dword v192, v[126:127], off offset:768
	global_load_dword v193, v[126:127], off offset:512
	s_lshl_b64 s[0:1], s[18:19], 11
	v_ashrrev_i32_e32 v7, 31, v6
	v_lshl_add_u64 v[128:129], v[4:5], 0, s[0:1]
	v_readlane_b32 s0, v254, 28
	v_add_u32_e32 v159, 0, v2
	v_lshlrev_b64 v[2:3], 11, v[6:7]
	v_readlane_b32 s1, v254, 29
	s_waitcnt lgkmcnt(0)
	s_ashr_i32 s27, s26, 31
	v_lshlrev_b64 v[102:103], 10, v[6:7]
	v_lshl_add_u64 v[2:3], s[0:1], 0, v[2:3]
	s_lshl_b64 s[0:1], s[26:27], 17
	v_writelane_b32 v255, s0, 5
	v_lshl_add_u64 v[130:131], v[2:3], 0, v[8:9]
	v_add_u32_e32 v12, 0, v12
	v_writelane_b32 v255, s1, 6
	v_readlane_b32 s0, v254, 36
	v_readlane_b32 s1, v254, 37
	v_lshl_add_u32 v13, v10, 2, s3
	v_mul_u32_u24_e32 v10, 0x90, v10
	v_lshl_add_u64 v[132:133], s[0:1], 0, v[102:103]
	s_mov_b32 s0, s26
	v_writelane_b32 v255, s0, 7
	v_lshl_add_u32 v14, v11, 4, 0
	v_mul_u32_u24_e32 v11, 0x1010, v11
	v_writelane_b32 v255, s1, 8
	s_lshl_b64 s[0:1], s[26:27], 16
	v_writelane_b32 v255, s0, 9
	v_mov_b64_e32 v[4:5], 0x20100
	v_cmp_eq_u32_e64 s[40:41], 0, v152
	v_writelane_b32 v255, s1, 10
	v_readlane_b32 s0, v254, 34
	v_readlane_b32 s1, v254, 35
	v_or_b32_e32 v155, 16, v154
	v_cmp_gt_u32_e64 s[42:43], 32, v152
	v_lshl_add_u64 v[2:3], s[0:1], 0, v[102:103]
	v_lshl_add_u64 v[2:3], v[2:3], 0, v[0:1]
	v_cmp_gt_u32_e64 s[44:45], 8, v152
	v_or_b32_e32 v156, 64, v152
	v_or_b32_e32 v157, 0x80, v152
	v_or_b32_e32 v158, 0xc0, v152
	v_add_u32_e32 v160, 0, v154
	v_lshl_add_u64 v[134:135], s[12:13], 0, v[0:1]
	v_lshl_add_u64 v[136:137], v[2:3], 1, v[4:5]
	v_add_u32_e32 v161, v14, v10
	v_add_u32_e32 v162, v13, v11
	v_add_u32_e32 v163, v12, v8
	v_readlane_b32 s62, v254, 32
	v_readlane_b32 s63, v254, 33
	s_branch .LBB0_1029

.LBB0_1049:
	s_lshl_b32 s3, s62, 6
	s_mov_b32 s11, 0
	s_waitcnt lgkmcnt(0)
	s_barrier
	ds_write_b32 v162, v2
	ds_write_b32 v162, v3 offset:1028
	ds_write_b32 v162, v4 offset:2056
	ds_write_b32 v162, v5 offset:3084
	ds_write_b32 v162, v6 offset:8224
	ds_write_b32 v162, v7 offset:9252
	ds_write_b32 v162, v8 offset:10280
	ds_write_b32 v162, v9 offset:11308
	ds_write_b32 v162, v10 offset:16448
	ds_write_b32 v162, v11 offset:17476
	ds_write_b32 v162, v12 offset:18504
	ds_write_b32 v162, v13 offset:19532
	ds_write_b32 v162, v14 offset:24672
	ds_write_b32 v162, v15 offset:25700
	ds_write_b32 v162, v16 offset:26728
	ds_write_b32 v162, v17 offset:27756
	ds_write_b32 v162, v18 offset:32896
	ds_write_b32 v162, v19 offset:33924
	ds_write_b32 v162, v20 offset:34952
	ds_write_b32 v162, v21 offset:35980
	ds_write_b32 v162, v22 offset:41120
	ds_write_b32 v162, v23 offset:42148
	ds_write_b32 v162, v24 offset:43176
	ds_write_b32 v162, v25 offset:44204
	ds_write_b32 v162, v26 offset:49344
	ds_write_b32 v162, v27 offset:50372
	ds_write_b32 v162, v28 offset:51400
	ds_write_b32 v162, v29 offset:52428
	ds_write_b32 v162, v30 offset:57568
	ds_write_b32 v162, v31 offset:58596
	ds_write_b32 v162, v32 offset:59624
	ds_write_b32 v162, v33 offset:60652
	s_waitcnt lgkmcnt(0)
	s_barrier
	s_waitcnt vmcnt(0)
	s_branch .LBB0_1051

.LBB0_1051:
	s_lshl_b32 s15, s11, 1
	s_add_i32 s15, s15, s18
	s_mul_i32 s0, s15, 0x404
	v_add_u32_e32 v11, s0, v159
	ds_read2st64_b32 v[2:3], v11 offset1:1
	v_mov_b32_e32 v12, v190
	v_mov_b32_e32 v13, v191
	v_mov_b32_e32 v18, v192
	v_add_u32_e32 v19, 4, v11
	s_waitcnt lgkmcnt(0)
	v_mul_f32_e32 v2, 0xbfb8aa3b, v2
	v_exp_f32_e32 v2, v2
	s_mov_b32 s19, 1
	v_add_f32_e32 v2, 1.0, v2
	v_div_scale_f32 v4, s[0:1], v2, v2, 1.0
	v_rcp_f32_e32 v5, v4
	s_nop 0
	v_fma_f32 v6, -v4, v5, 1.0
	v_fmac_f32_e32 v5, v6, v5
	v_div_scale_f32 v6, vcc, 1.0, v2, 1.0
	v_mul_f32_e32 v7, v6, v5
	v_fma_f32 v8, -v4, v7, v6
	v_fmac_f32_e32 v7, v8, v5
	v_fma_f32 v4, -v4, v7, v6
	v_div_fmas_f32 v4, v4, v5, v7
	v_div_fixup_f32 v7, v4, v2, 1.0
	v_mul_f32_e32 v2, 0xbfb8aa3b, v3
	v_exp_f32_e32 v2, v2
	s_nop 0
	v_add_f32_e32 v2, 1.0, v2
	v_div_scale_f32 v3, s[0:1], v2, v2, 1.0
	v_rcp_f32_e32 v5, v3
	s_nop 0
	v_fma_f32 v6, -v3, v5, 1.0
	v_fmac_f32_e32 v5, v6, v5
	v_div_scale_f32 v6, vcc, 1.0, v2, 1.0
	v_mul_f32_e32 v8, v6, v5
	v_fma_f32 v9, -v3, v8, v6
	v_fmac_f32_e32 v8, v9, v5
	v_fma_f32 v3, -v3, v8, v6
	v_div_fmas_f32 v3, v3, v5, v8
	v_div_fixup_f32 v8, v3, v2, 1.0
	ds_read2st64_b32 v[2:3], v11 offset0:2 offset1:3
	s_waitcnt lgkmcnt(0)
	v_mul_f32_e32 v2, 0xbfb8aa3b, v2
	v_exp_f32_e32 v2, v2
	s_nop 0
	v_add_f32_e32 v2, 1.0, v2
	v_div_scale_f32 v6, s[0:1], v2, v2, 1.0
	v_rcp_f32_e32 v9, v6
	s_nop 0
	v_fma_f32 v10, -v6, v9, 1.0
	v_fmac_f32_e32 v9, v10, v9
	v_div_scale_f32 v10, vcc, 1.0, v2, 1.0
	v_mul_f32_e32 v14, v10, v9
	v_fma_f32 v15, -v6, v14, v10
	v_fmac_f32_e32 v14, v15, v9
	v_fma_f32 v6, -v6, v14, v10
	v_div_fmas_f32 v6, v6, v9, v14
	v_div_fixup_f32 v9, v6, v2, 1.0
	v_mul_f32_e32 v2, 0xbfb8aa3b, v3
	v_exp_f32_e32 v2, v2
	v_mov_b32_e32 v14, v193
	v_add_f32_e32 v2, 1.0, v2
	v_div_scale_f32 v3, s[0:1], v2, v2, 1.0
	v_rcp_f32_e32 v10, v3
	v_add_f32_e32 v4, v12, v7
	v_add_f32_e32 v5, v13, v8
	v_fma_f32 v15, -v3, v10, 1.0
	v_fmac_f32_e32 v10, v15, v10
	v_div_scale_f32 v15, vcc, 1.0, v2, 1.0
	v_mul_f32_e32 v16, v15, v10
	v_fma_f32 v17, -v3, v16, v15
	v_fmac_f32_e32 v16, v17, v10
	v_fma_f32 v3, -v3, v16, v15
	v_div_fmas_f32 v3, v3, v10, v16
	v_div_fixup_f32 v10, v3, v2, 1.0
	ds_read2st64_b32 v[2:3], v19 offset0:4 offset1:5
	v_add_f32_e32 v15, v18, v10
	s_waitcnt lgkmcnt(0)
	v_mul_f32_e32 v2, 0xbfb8aa3b, v2
	v_exp_f32_e32 v2, v2
	v_add_f32_e32 v6, v14, v9
	v_add_f32_e32 v2, 1.0, v2
	v_div_scale_f32 v11, s[0:1], v2, v2, 1.0
	v_rcp_f32_e32 v16, v11
	s_nop 0
	v_fma_f32 v17, -v11, v16, 1.0
	v_fmac_f32_e32 v16, v17, v16
	v_div_scale_f32 v17, vcc, 1.0, v2, 1.0
	v_mul_f32_e32 v20, v17, v16
	v_fma_f32 v21, -v11, v20, v17
	v_fmac_f32_e32 v20, v21, v16
	v_fma_f32 v11, -v11, v20, v17
	v_div_fmas_f32 v11, v11, v16, v20
	v_div_fixup_f32 v11, v11, v2, 1.0
	v_mul_f32_e32 v2, 0xbfb8aa3b, v3
	v_exp_f32_e32 v2, v2
	v_add_f32_e32 v16, v12, v11
	v_add_f32_e32 v2, 1.0, v2
	v_div_scale_f32 v3, s[0:1], v2, v2, 1.0
	v_rcp_f32_e32 v12, v3
	s_nop 0
	v_fma_f32 v17, -v3, v12, 1.0
	v_fmac_f32_e32 v12, v17, v12
	v_div_scale_f32 v17, vcc, 1.0, v2, 1.0
	v_mul_f32_e32 v20, v17, v12
	v_fma_f32 v21, -v3, v20, v17
	v_fmac_f32_e32 v20, v21, v12
	v_fma_f32 v3, -v3, v20, v17
	v_div_fmas_f32 v3, v3, v12, v20
	v_div_fixup_f32 v12, v3, v2, 1.0
	ds_read2st64_b32 v[2:3], v19 offset0:6 offset1:7
	v_add_f32_e32 v17, v13, v12
	s_waitcnt lgkmcnt(0)
	v_mul_f32_e32 v2, 0xbfb8aa3b, v2
	v_exp_f32_e32 v2, v2
	s_nop 0
	v_add_f32_e32 v2, 1.0, v2
	v_div_scale_f32 v13, s[0:1], v2, v2, 1.0
	v_rcp_f32_e32 v19, v13
	s_nop 0
	v_fma_f32 v20, -v13, v19, 1.0
	v_fmac_f32_e32 v19, v20, v19
	v_div_scale_f32 v20, vcc, 1.0, v2, 1.0
	v_mul_f32_e32 v21, v20, v19
	v_fma_f32 v22, -v13, v21, v20
	v_fmac_f32_e32 v21, v22, v19
	v_fma_f32 v13, -v13, v21, v20
	v_div_fmas_f32 v13, v13, v19, v21
	v_div_fixup_f32 v13, v13, v2, 1.0
	v_mul_f32_e32 v2, 0xbfb8aa3b, v3
	v_exp_f32_e32 v2, v2
	v_add_f32_e32 v19, v14, v13
	v_add_f32_e32 v2, 1.0, v2
	v_div_scale_f32 v3, s[0:1], v2, v2, 1.0
	v_rcp_f32_e32 v14, v3
	s_nop 0
	v_fma_f32 v20, -v3, v14, 1.0
	v_fmac_f32_e32 v14, v20, v14
	v_div_scale_f32 v20, vcc, 1.0, v2, 1.0
	v_mul_f32_e32 v21, v20, v14
	v_fma_f32 v22, -v3, v21, v20
	v_fmac_f32_e32 v21, v22, v14
	v_fma_f32 v3, -v3, v21, v20
	v_div_fmas_f32 v3, v3, v14, v21
	v_div_fixup_f32 v14, v3, v2, 1.0
	v_mov_b32_dpp v2, v4 quad_perm:[1,0,3,2] row_mask:0xf bank_mask:0xf bound_ctrl:1
	v_max_f32_e32 v2, v2, v2
	v_max_f32_e32 v2, v4, v2
	v_add_f32_e32 v18, v18, v14
	s_nop 0
	v_mov_b32_dpp v3, v2 quad_perm:[2,3,0,1] row_mask:0xf bank_mask:0xf bound_ctrl:1
	v_max_f32_e32 v3, v3, v3
	v_max_f32_e32 v2, v2, v3
	s_nop 1
	v_mov_b32_dpp v3, v2 row_half_mirror row_mask:0xf bank_mask:0xf bound_ctrl:1
	v_max_f32_e32 v3, v3, v3
	v_max_f32_e32 v2, v2, v3
	s_nop 1
	v_mov_b32_dpp v3, v2 row_mirror row_mask:0xf bank_mask:0xf bound_ctrl:1
	v_max_f32_e32 v3, v3, v3
	v_max_f32_e32 v3, v2, v3
	s_nop 0
	v_readlane_b32 s0, v3, 0
	v_readlane_b32 s1, v3, 16
	s_nop 0
	v_max_f32_e64 v20, s0, s0
	v_max_f32_e64 v2, s1, s1
	v_readlane_b32 s0, v3, 32
	v_readlane_b32 s1, v3, 48
	v_max_f32_e32 v2, v20, v2
	v_max_f32_e64 v20, s0, s0
	v_max_f32_e64 v3, s1, s1
	v_max_f32_e32 v21, v20, v3
	v_cndmask_b32_e64 v3, v21, v2, s[42:43]
	v_cmp_eq_f32_e32 vcc, v4, v3
	s_ff1_i32_b32 s8, vcc_hi
	s_ff1_i32_b32 s0, vcc_lo
	s_or_b32 s8, s8, 32
	v_cmp_eq_u32_e64 s[0:1], s0, v152
	v_cmp_eq_u32_e32 vcc, s8, v152
	s_or_b64 vcc, s[0:1], vcc
	s_nop 0
	v_cndmask_b32_e32 v3, v4, v228, vcc
	s_nop 1
	v_mov_b32_dpp v20, v3 quad_perm:[1,0,3,2] row_mask:0xf bank_mask:0xf bound_ctrl:1
	v_max_f32_e32 v20, v20, v20
	v_max_f32_e32 v3, v3, v20
	s_nop 1
	v_mov_b32_dpp v20, v3 quad_perm:[2,3,0,1] row_mask:0xf bank_mask:0xf bound_ctrl:1
	v_max_f32_e32 v20, v20, v20
	v_max_f32_e32 v3, v3, v20
	s_nop 1
	v_mov_b32_dpp v20, v3 row_half_mirror row_mask:0xf bank_mask:0xf bound_ctrl:1
	v_max_f32_e32 v20, v20, v20
	v_max_f32_e32 v3, v3, v20
	s_nop 1
	v_mov_b32_dpp v20, v3 row_mirror row_mask:0xf bank_mask:0xf bound_ctrl:1
	v_max_f32_e32 v20, v20, v20
	v_max_f32_e32 v3, v3, v20
	s_nop 0
	v_readlane_b32 s0, v3, 0
	v_readlane_b32 s1, v3, 16
	s_nop 0
	v_max_f32_e64 v22, s0, s0
	v_max_f32_e64 v20, s1, s1
	v_readlane_b32 s0, v3, 32
	v_readlane_b32 s1, v3, 48
	v_max_f32_e32 v20, v22, v20
	v_max_f32_e64 v22, s0, s0
	v_max_f32_e64 v3, s1, s1
	v_max_f32_e32 v3, v22, v3
	v_pk_add_f32 v[2:3], v[20:21], v[2:3]
	v_mov_b32_dpp v20, v16 quad_perm:[1,0,3,2] row_mask:0xf bank_mask:0xf bound_ctrl:1
	v_max_f32_e32 v20, v20, v20
	v_max_f32_e32 v20, v16, v20
	s_nop 1
	v_mov_b32_dpp v21, v20 quad_perm:[2,3,0,1] row_mask:0xf bank_mask:0xf bound_ctrl:1
	v_max_f32_e32 v21, v21, v21
	v_max_f32_e32 v20, v20, v21
	s_nop 1
	v_mov_b32_dpp v21, v20 row_half_mirror row_mask:0xf bank_mask:0xf bound_ctrl:1
	v_max_f32_e32 v21, v21, v21
	v_max_f32_e32 v20, v20, v21
	s_nop 1
	v_mov_b32_dpp v21, v20 row_mirror row_mask:0xf bank_mask:0xf bound_ctrl:1
	v_max_f32_e32 v21, v21, v21
	v_max_f32_e32 v20, v20, v21
	s_nop 0
	v_readlane_b32 s0, v20, 0
	v_readlane_b32 s1, v20, 16
	s_nop 0
	v_max_f32_e64 v22, s0, s0
	v_max_f32_e64 v21, s1, s1
	v_readlane_b32 s0, v20, 32
	v_readlane_b32 s1, v20, 48
	v_max_f32_e32 v28, v22, v21
	v_max_f32_e64 v21, s0, s0
	v_max_f32_e64 v20, s1, s1
	v_max_f32_e32 v29, v21, v20
	v_cndmask_b32_e64 v20, v29, v28, s[42:43]
	v_cmp_eq_f32_e32 vcc, v16, v20
	s_ff1_i32_b32 s8, vcc_hi
	s_ff1_i32_b32 s0, vcc_lo
	s_or_b32 s8, s8, 32
	v_cmp_eq_u32_e64 s[0:1], s0, v152
	v_cmp_eq_u32_e32 vcc, s8, v152
	s_or_b64 vcc, s[0:1], vcc
	s_nop 0
	v_cndmask_b32_e32 v20, v16, v228, vcc
	s_nop 1
	v_mov_b32_dpp v21, v20 quad_perm:[1,0,3,2] row_mask:0xf bank_mask:0xf bound_ctrl:1
	v_max_f32_e32 v21, v21, v21
	v_max_f32_e32 v20, v20, v21
	s_nop 1
	v_mov_b32_dpp v21, v20 quad_perm:[2,3,0,1] row_mask:0xf bank_mask:0xf bound_ctrl:1
	v_max_f32_e32 v21, v21, v21
	v_max_f32_e32 v20, v20, v21
	s_nop 1
	v_mov_b32_dpp v21, v20 row_half_mirror row_mask:0xf bank_mask:0xf bound_ctrl:1
	v_max_f32_e32 v21, v21, v21
	v_max_f32_e32 v20, v20, v21
	s_nop 1
	v_mov_b32_dpp v21, v20 row_mirror row_mask:0xf bank_mask:0xf bound_ctrl:1
	v_max_f32_e32 v21, v21, v21
	v_max_f32_e32 v20, v20, v21
	s_nop 0
	v_readlane_b32 s69, v20, 0
	v_readlane_b32 s77, v20, 16
	v_readlane_b32 s68, v20, 32
	v_readlane_b32 s70, v20, 48
	v_mov_b32_dpp v20, v5 quad_perm:[1,0,3,2] row_mask:0xf bank_mask:0xf bound_ctrl:1
	v_max_f32_e32 v20, v20, v20
	v_max_f32_e32 v20, v5, v20
	s_nop 1
	v_mov_b32_dpp v21, v20 quad_perm:[2,3,0,1] row_mask:0xf bank_mask:0xf bound_ctrl:1
	v_max_f32_e32 v21, v21, v21
	v_max_f32_e32 v20, v20, v21
	s_nop 1
	v_mov_b32_dpp v21, v20 row_half_mirror row_mask:0xf bank_mask:0xf bound_ctrl:1
	v_max_f32_e32 v21, v21, v21
	v_max_f32_e32 v20, v20, v21
	s_nop 1
	v_mov_b32_dpp v21, v20 row_mirror row_mask:0xf bank_mask:0xf bound_ctrl:1
	v_max_f32_e32 v21, v21, v21
	v_max_f32_e32 v21, v20, v21
	s_nop 0
	v_readlane_b32 s0, v21, 0
	v_readlane_b32 s1, v21, 16
	s_nop 0
	v_max_f32_e64 v22, s0, s0
	v_max_f32_e64 v20, s1, s1
	v_readlane_b32 s0, v21, 32
	v_readlane_b32 s1, v21, 48
	v_max_f32_e32 v20, v22, v20
	v_max_f32_e64 v22, s0, s0
	v_max_f32_e64 v21, s1, s1
	v_max_f32_e32 v21, v22, v21
	v_cndmask_b32_e64 v22, v21, v20, s[42:43]
	v_cmp_eq_f32_e32 vcc, v5, v22
	s_ff1_i32_b32 s8, vcc_hi
	s_ff1_i32_b32 s0, vcc_lo
	s_or_b32 s8, s8, 32
	v_cmp_eq_u32_e64 s[0:1], s0, v152
	v_cmp_eq_u32_e32 vcc, s8, v152
	s_or_b64 vcc, s[0:1], vcc
	s_nop 0
	v_cndmask_b32_e32 v22, v5, v228, vcc
	s_nop 1
	v_mov_b32_dpp v23, v22 quad_perm:[1,0,3,2] row_mask:0xf bank_mask:0xf bound_ctrl:1
	v_max_f32_e32 v23, v23, v23
	v_max_f32_e32 v22, v22, v23
	s_nop 1
	v_mov_b32_dpp v23, v22 quad_perm:[2,3,0,1] row_mask:0xf bank_mask:0xf bound_ctrl:1
	v_max_f32_e32 v23, v23, v23
	v_max_f32_e32 v22, v22, v23
	s_nop 1
	v_mov_b32_dpp v23, v22 row_half_mirror row_mask:0xf bank_mask:0xf bound_ctrl:1
	v_max_f32_e32 v23, v23, v23
	v_max_f32_e32 v22, v22, v23
	s_nop 1
	v_mov_b32_dpp v23, v22 row_mirror row_mask:0xf bank_mask:0xf bound_ctrl:1
	v_max_f32_e32 v23, v23, v23
	v_max_f32_e32 v22, v22, v23
	s_nop 0
	v_readlane_b32 s8, v22, 0
	v_readlane_b32 s9, v22, 16
	v_readlane_b32 s26, v22, 32
	v_readlane_b32 s27, v22, 48
	v_mov_b32_dpp v22, v17 quad_perm:[1,0,3,2] row_mask:0xf bank_mask:0xf bound_ctrl:1
	v_max_f32_e32 v22, v22, v22
	v_max_f32_e32 v22, v17, v22
	s_nop 1
	v_mov_b32_dpp v23, v22 quad_perm:[2,3,0,1] row_mask:0xf bank_mask:0xf bound_ctrl:1
	v_max_f32_e32 v23, v23, v23
	v_max_f32_e32 v22, v22, v23
	s_nop 1
	v_mov_b32_dpp v23, v22 row_half_mirror row_mask:0xf bank_mask:0xf bound_ctrl:1
	v_max_f32_e32 v23, v23, v23
	v_max_f32_e32 v22, v22, v23
	s_nop 1
	v_mov_b32_dpp v23, v22 row_mirror row_mask:0xf bank_mask:0xf bound_ctrl:1
	v_max_f32_e32 v23, v23, v23
	v_max_f32_e32 v22, v22, v23
	s_nop 0
	v_readlane_b32 s0, v22, 0
	v_readlane_b32 s1, v22, 16
	s_nop 0
	v_max_f32_e64 v24, s0, s0
	v_max_f32_e64 v23, s1, s1
	v_readlane_b32 s0, v22, 32
	v_readlane_b32 s1, v22, 48
	v_max_f32_e32 v33, v24, v23
	v_max_f32_e64 v23, s0, s0
	v_max_f32_e64 v22, s1, s1
	v_max_f32_e32 v32, v23, v22
	v_cndmask_b32_e64 v22, v32, v33, s[42:43]
	v_cmp_eq_f32_e32 vcc, v17, v22
	s_ff1_i32_b32 s14, vcc_hi
	s_ff1_i32_b32 s0, vcc_lo
	s_or_b32 s14, s14, 32
	v_cmp_eq_u32_e64 s[0:1], s0, v152
	v_cmp_eq_u32_e32 vcc, s14, v152
	s_or_b64 vcc, s[0:1], vcc
	s_nop 0
	v_cndmask_b32_e32 v22, v17, v228, vcc
	s_nop 1
	v_mov_b32_dpp v23, v22 quad_perm:[1,0,3,2] row_mask:0xf bank_mask:0xf bound_ctrl:1
	v_max_f32_e32 v23, v23, v23
	v_max_f32_e32 v22, v22, v23
	s_nop 1
	v_mov_b32_dpp v23, v22 quad_perm:[2,3,0,1] row_mask:0xf bank_mask:0xf bound_ctrl:1
	v_max_f32_e32 v23, v23, v23
	v_max_f32_e32 v22, v22, v23
	s_nop 1
	v_mov_b32_dpp v23, v22 row_half_mirror row_mask:0xf bank_mask:0xf bound_ctrl:1
	v_max_f32_e32 v23, v23, v23
	v_max_f32_e32 v22, v22, v23
	s_nop 1
	v_mov_b32_dpp v23, v22 row_mirror row_mask:0xf bank_mask:0xf bound_ctrl:1
	v_max_f32_e32 v23, v23, v23
	v_max_f32_e32 v22, v22, v23
	s_nop 0
	v_readlane_b32 s88, v22, 0
	v_readlane_b32 s89, v22, 16
	v_readlane_b32 s83, v22, 32
	v_readlane_b32 s84, v22, 48
	v_mov_b32_dpp v22, v6 quad_perm:[1,0,3,2] row_mask:0xf bank_mask:0xf bound_ctrl:1
	v_max_f32_e32 v22, v22, v22
	v_max_f32_e32 v22, v6, v22
	s_nop 1
	v_mov_b32_dpp v23, v22 quad_perm:[2,3,0,1] row_mask:0xf bank_mask:0xf bound_ctrl:1
	v_max_f32_e32 v23, v23, v23
	v_max_f32_e32 v22, v22, v23
	s_nop 1
	v_mov_b32_dpp v23, v22 row_half_mirror row_mask:0xf bank_mask:0xf bound_ctrl:1
	v_max_f32_e32 v23, v23, v23
	v_max_f32_e32 v22, v22, v23
	s_nop 1
	v_mov_b32_dpp v23, v22 row_mirror row_mask:0xf bank_mask:0xf bound_ctrl:1
	v_max_f32_e32 v23, v23, v23
	v_max_f32_e32 v23, v22, v23
	s_nop 0
	v_readlane_b32 s0, v23, 0
	v_readlane_b32 s1, v23, 16
	s_nop 0
	v_max_f32_e64 v24, s0, s0
	v_max_f32_e64 v22, s1, s1
	v_readlane_b32 s0, v23, 32
	v_readlane_b32 s1, v23, 48
	v_max_f32_e32 v22, v24, v22
	v_max_f32_e64 v24, s0, s0
	v_max_f32_e64 v23, s1, s1
	v_max_f32_e32 v23, v24, v23
	v_cndmask_b32_e64 v24, v23, v22, s[42:43]
	v_cmp_eq_f32_e32 vcc, v6, v24
	s_ff1_i32_b32 s14, vcc_hi
	s_ff1_i32_b32 s0, vcc_lo
	s_or_b32 s14, s14, 32
	v_cmp_eq_u32_e64 s[0:1], s0, v152
	v_cmp_eq_u32_e32 vcc, s14, v152
	s_or_b64 vcc, s[0:1], vcc
	s_nop 0
	v_cndmask_b32_e32 v24, v6, v228, vcc
	s_nop 1
	v_mov_b32_dpp v25, v24 quad_perm:[1,0,3,2] row_mask:0xf bank_mask:0xf bound_ctrl:1
	v_max_f32_e32 v25, v25, v25
	v_max_f32_e32 v24, v24, v25
	s_nop 1
	v_mov_b32_dpp v25, v24 quad_perm:[2,3,0,1] row_mask:0xf bank_mask:0xf bound_ctrl:1
	v_max_f32_e32 v25, v25, v25
	v_max_f32_e32 v24, v24, v25
	s_nop 1
	v_mov_b32_dpp v25, v24 row_half_mirror row_mask:0xf bank_mask:0xf bound_ctrl:1
	v_max_f32_e32 v25, v25, v25
	v_max_f32_e32 v24, v24, v25
	s_nop 1
	v_mov_b32_dpp v25, v24 row_mirror row_mask:0xf bank_mask:0xf bound_ctrl:1
	v_max_f32_e32 v25, v25, v25
	v_max_f32_e32 v24, v24, v25
	s_nop 0
	v_readlane_b32 s29, v24, 0
	v_readlane_b32 s33, v24, 16
	v_readlane_b32 s38, v24, 32
	v_readlane_b32 s39, v24, 48
	v_mov_b32_dpp v24, v19 quad_perm:[1,0,3,2] row_mask:0xf bank_mask:0xf bound_ctrl:1
	v_max_f32_e32 v24, v24, v24
	v_max_f32_e32 v24, v19, v24
	s_nop 1
	v_mov_b32_dpp v25, v24 quad_perm:[2,3,0,1] row_mask:0xf bank_mask:0xf bound_ctrl:1
	v_max_f32_e32 v25, v25, v25
	v_max_f32_e32 v24, v24, v25
	s_nop 1
	v_mov_b32_dpp v25, v24 row_half_mirror row_mask:0xf bank_mask:0xf bound_ctrl:1
	v_max_f32_e32 v25, v25, v25
	v_max_f32_e32 v24, v24, v25
	s_nop 1
	v_mov_b32_dpp v25, v24 row_mirror row_mask:0xf bank_mask:0xf bound_ctrl:1
	v_max_f32_e32 v25, v25, v25
	v_max_f32_e32 v24, v24, v25
	s_nop 0
	v_readlane_b32 s0, v24, 0
	v_readlane_b32 s1, v24, 16
	s_nop 0
	v_max_f32_e64 v26, s0, s0
	v_max_f32_e64 v25, s1, s1
	v_readlane_b32 s0, v24, 32
	v_readlane_b32 s1, v24, 48
	v_max_f32_e32 v31, v26, v25
	v_max_f32_e64 v25, s0, s0
	v_max_f32_e64 v24, s1, s1
	v_max_f32_e32 v30, v25, v24
	v_cndmask_b32_e64 v24, v30, v31, s[42:43]
	v_cmp_eq_f32_e32 vcc, v19, v24
	s_ff1_i32_b32 s14, vcc_hi
	s_ff1_i32_b32 s0, vcc_lo
	s_or_b32 s14, s14, 32
	v_cmp_eq_u32_e64 s[0:1], s0, v152
	v_cmp_eq_u32_e32 vcc, s14, v152
	s_or_b64 vcc, s[0:1], vcc
	s_nop 0
	v_cndmask_b32_e32 v24, v19, v228, vcc
	s_nop 1
	v_mov_b32_dpp v25, v24 quad_perm:[1,0,3,2] row_mask:0xf bank_mask:0xf bound_ctrl:1
	v_max_f32_e32 v25, v25, v25
	v_max_f32_e32 v24, v24, v25
	s_nop 1
	v_mov_b32_dpp v25, v24 quad_perm:[2,3,0,1] row_mask:0xf bank_mask:0xf bound_ctrl:1
	v_max_f32_e32 v25, v25, v25
	v_max_f32_e32 v24, v24, v25
	s_nop 1
	v_mov_b32_dpp v25, v24 row_half_mirror row_mask:0xf bank_mask:0xf bound_ctrl:1
	v_max_f32_e32 v25, v25, v25
	v_max_f32_e32 v24, v24, v25
	s_nop 1
	v_mov_b32_dpp v25, v24 row_mirror row_mask:0xf bank_mask:0xf bound_ctrl:1
	v_max_f32_e32 v25, v25, v25
	v_max_f32_e32 v24, v24, v25
	s_nop 0
	v_readlane_b32 s80, v24, 0
	v_readlane_b32 s82, v24, 16
	v_readlane_b32 s76, v24, 32
	v_readlane_b32 s78, v24, 48
	v_mov_b32_dpp v24, v15 quad_perm:[1,0,3,2] row_mask:0xf bank_mask:0xf bound_ctrl:1
	v_max_f32_e32 v24, v24, v24
	v_max_f32_e32 v24, v15, v24
	s_nop 1
	v_mov_b32_dpp v25, v24 quad_perm:[2,3,0,1] row_mask:0xf bank_mask:0xf bound_ctrl:1
	v_max_f32_e32 v25, v25, v25
	v_max_f32_e32 v24, v24, v25
	s_nop 1
	v_mov_b32_dpp v25, v24 row_half_mirror row_mask:0xf bank_mask:0xf bound_ctrl:1
	v_max_f32_e32 v25, v25, v25
	v_max_f32_e32 v24, v24, v25
	s_nop 1
	v_mov_b32_dpp v25, v24 row_mirror row_mask:0xf bank_mask:0xf bound_ctrl:1
	v_max_f32_e32 v25, v25, v25
	v_max_f32_e32 v25, v24, v25
	s_nop 0
	v_readlane_b32 s0, v25, 0
	v_readlane_b32 s1, v25, 16
	s_nop 0
	v_max_f32_e64 v26, s0, s0
	v_max_f32_e64 v24, s1, s1
	v_readlane_b32 s0, v25, 32
	v_readlane_b32 s1, v25, 48
	v_max_f32_e32 v24, v26, v24
	v_max_f32_e64 v26, s0, s0
	v_max_f32_e64 v25, s1, s1
	v_max_f32_e32 v26, v26, v25
	v_cndmask_b32_e64 v25, v26, v24, s[42:43]
	v_cmp_eq_f32_e32 vcc, v15, v25
	s_ff1_i32_b32 s14, vcc_hi
	s_ff1_i32_b32 s0, vcc_lo
	s_or_b32 s14, s14, 32
	v_cmp_eq_u32_e64 s[0:1], s0, v152
	v_cmp_eq_u32_e32 vcc, s14, v152
	s_or_b64 vcc, s[0:1], vcc
	s_nop 0
	v_cndmask_b32_e32 v25, v15, v228, vcc
	s_nop 1
	v_mov_b32_dpp v27, v25 quad_perm:[1,0,3,2] row_mask:0xf bank_mask:0xf bound_ctrl:1
	v_max_f32_e32 v27, v27, v27
	v_max_f32_e32 v25, v25, v27
	s_nop 1
	v_mov_b32_dpp v27, v25 quad_perm:[2,3,0,1] row_mask:0xf bank_mask:0xf bound_ctrl:1
	v_max_f32_e32 v27, v27, v27
	v_max_f32_e32 v25, v25, v27
	s_nop 1
	v_mov_b32_dpp v27, v25 row_half_mirror row_mask:0xf bank_mask:0xf bound_ctrl:1
	v_max_f32_e32 v27, v27, v27
	v_max_f32_e32 v25, v25, v27
	s_nop 1
	v_mov_b32_dpp v27, v25 row_mirror row_mask:0xf bank_mask:0xf bound_ctrl:1
	v_max_f32_e32 v27, v27, v27
	v_max_f32_e32 v25, v25, v27
	s_nop 0
	v_readlane_b32 s66, v25, 0
	v_readlane_b32 s67, v25, 16
	v_readlane_b32 s64, v25, 32
	v_readlane_b32 s65, v25, 48
	v_mov_b32_dpp v25, v18 quad_perm:[1,0,3,2] row_mask:0xf bank_mask:0xf bound_ctrl:1
	v_max_f32_e32 v25, v25, v25
	v_max_f32_e32 v25, v18, v25
	s_nop 1
	v_mov_b32_dpp v27, v25 quad_perm:[2,3,0,1] row_mask:0xf bank_mask:0xf bound_ctrl:1
	v_max_f32_e32 v27, v27, v27
	v_max_f32_e32 v25, v25, v27
	s_nop 1
	v_mov_b32_dpp v27, v25 row_half_mirror row_mask:0xf bank_mask:0xf bound_ctrl:1
	v_max_f32_e32 v27, v27, v27
	v_max_f32_e32 v25, v25, v27
	s_nop 1
	v_mov_b32_dpp v27, v25 row_mirror row_mask:0xf bank_mask:0xf bound_ctrl:1
	v_max_f32_e32 v27, v27, v27
	v_max_f32_e32 v25, v25, v27
	s_nop 0
	v_readlane_b32 s0, v25, 0
	v_readlane_b32 s1, v25, 16
	s_nop 0
	v_max_f32_e64 v34, s0, s0
	v_max_f32_e64 v27, s1, s1
	v_readlane_b32 s0, v25, 32
	v_readlane_b32 s1, v25, 48
	v_max_f32_e32 v27, v34, v27
	v_max_f32_e64 v34, s0, s0
	v_max_f32_e64 v25, s1, s1
	v_max_f32_e32 v25, v34, v25
	v_cndmask_b32_e64 v34, v25, v27, s[42:43]
	v_cmp_eq_f32_e32 vcc, v18, v34
	s_ff1_i32_b32 s14, vcc_hi
	s_ff1_i32_b32 s0, vcc_lo
	s_or_b32 s14, s14, 32
	v_cmp_eq_u32_e64 s[0:1], s0, v152
	v_cmp_eq_u32_e32 vcc, s14, v152
	s_or_b64 vcc, s[0:1], vcc
	s_mov_b32 s0, 1
	v_cndmask_b32_e32 v34, v18, v228, vcc
	v_cmp_gt_f32_e32 vcc, v2, v3
	s_and_b64 vcc, exec, vcc
	v_mov_b32_dpp v35, v34 quad_perm:[1,0,3,2] row_mask:0xf bank_mask:0xf bound_ctrl:1
	v_max_f32_e32 v35, v35, v35
	v_max_f32_e32 v34, v34, v35
	s_nop 1
	v_mov_b32_dpp v35, v34 quad_perm:[2,3,0,1] row_mask:0xf bank_mask:0xf bound_ctrl:1
	v_max_f32_e32 v35, v35, v35
	v_max_f32_e32 v34, v34, v35
	s_nop 1
	v_mov_b32_dpp v35, v34 row_half_mirror row_mask:0xf bank_mask:0xf bound_ctrl:1
	v_max_f32_e32 v35, v35, v35
	v_max_f32_e32 v34, v34, v35
	s_nop 1
	v_mov_b32_dpp v35, v34 row_mirror row_mask:0xf bank_mask:0xf bound_ctrl:1
	v_max_f32_e32 v35, v35, v35
	v_max_f32_e32 v34, v34, v35
	s_nop 0
	v_readlane_b32 s56, v34, 0
	v_readlane_b32 s63, v34, 16
	v_readlane_b32 s54, v34, 32
	v_readlane_b32 s55, v34, 48
	s_cbranch_vccnz .LBB0_1054
	v_cmp_neq_f32_e32 vcc, v2, v3
	s_cbranch_vccz .LBB0_1054
	s_mov_b32 s0, 0
